# baseline (speedup 1.0000x reference)
.Lagg_join_1:
	v_cmp_gt_u32_e32 vcc, s5, v2
	s_and_saveexec_b64 s[58:59], vcc
	v_add_u32_e32 v61, s6, v2
	v_mad_u32_u24 v40, v61, s46, v1
	global_load_dwordx4 v[24:27], v40, s[70:71] nt
	global_load_dwordx4 v[28:31], v40, s[70:71] offset:64 nt
	v_lshlrev_b32_e32 v41, 9, v61
	v_lshl_add_u32 v41, v1, 0, v41
	s_mov_b64 exec, s[58:59]
	s_waitcnt lgkmcnt(0)
	s_barrier
	v_cmp_gt_u32_e32 vcc, s5, v2
	s_and_saveexec_b64 s[58:59], vcc
	v_lshlrev_b32_e32 v61, 2, v0
	v_add_u32_e32 v60, 0x6e40, v61
	ds_read_b32 v48, v61 offset:24448
	ds_read_b32 v49, v61 offset:27584
	ds_read_b32 v50, v61 offset:30720
	ds_read_b32 v51, v61 offset:33856
	ds_read_b32 v52, v61 offset:36992
	ds_read_b32 v53, v61 offset:40128
	ds_read_b32 v54, v61 offset:43264
	ds_read_b32 v55, v61 offset:46400
	ds_read_b32 v45, v61 offset:49536
	s_waitcnt lgkmcnt(6)
	ds_read_b32 v32, v60 offset:24448
	ds_read_b32 v33, v60 offset:27584
	ds_read_b32 v34, v60 offset:30720
	ds_read_b32 v35, v60 offset:33856
	ds_read_b32 v36, v60 offset:36992
	ds_read_b32 v37, v60 offset:40128
	ds_read_b32 v38, v60 offset:43264
	ds_read_b32 v39, v60 offset:46400
	ds_read_b32 v56, v60 offset:49536
	v_mov_b32_e32 v62, 0x3c003c00
	s_waitcnt lgkmcnt(0)
	v_pk_fma_f16 v48, v32, v62, v48
	v_pk_fma_f16 v49, v33, v62, v49
	v_pk_fma_f16 v50, v34, v62, v50
	v_pk_fma_f16 v51, v35, v62, v51
	v_pk_fma_f16 v52, v36, v62, v52
	v_pk_fma_f16 v53, v37, v62, v53
	v_pk_fma_f16 v54, v38, v62, v54
	v_pk_fma_f16 v55, v39, v62, v55
	v_add_f32_e32 v45, v45, v56
	s_cbranch_execz .Lagg_end_1
	v_add_f32_e32 v47, v46, v4
	v_mul_f32_e32 v58, 0x3c23d70a, v47
	v_max_f32_e32 v47, v47, v58
	v_sub_f32_e32 v58, v14, v47
	v_exp_f32_e32 v58, v58
	v_mul_f32_e32 v59, 0x33000000, v45
	v_rcp_f32_e32 v42, v45
	v_mul_f32_e32 v58, 0x24e69595, v58
	v_fma_f32 v60, -v45, v42, 1.0
	v_cmp_ge_f32_e64 s[62:63], v59, v58
	v_cmp_eq_f32_e32 vcc, 0, v45
	v_fmac_f32_e32 v42, v60, v42
	s_nop 1
	v_cndmask_b32_e64 v42, v42, 0, vcc
	s_or_b64 s[62:63], s[62:63], vcc
	s_mov_b64 s[66:67], exec
	s_andn2_b64 exec, exec, s[62:63]
	s_cbranch_execnz .Lagg_gmax_1
